# waitcnt placement (strategy 1): weight-conversion loops (P0 x2, P3) no longer wait vmcnt(0) on the next item's just-issued prefetch (false dependency through the unused high half of op_sel_hi:[1,0] pk
# speedup vs baseline: 1.0007x; 1.0007x over previous
.LBB0_98:
	v_pk_mul_f32 v[86:87], v[86:87], v[94:95] op_sel_hi:[1,0]
	v_add_u32_e32 v38, 0x8000, v57
	v_pk_mul_f32 v[84:85], v[84:85], v[94:95] op_sel_hi:[1,0]
	ds_write2_b32 v38, v86, v87 offset1:1
	v_add_u32_e32 v38, 0x8008, v57
	ds_write2_b32 v38, v84, v85 offset1:1
	v_pk_mul_f32 v[80:81], v[80:81], v[92:93] op_sel_hi:[1,0]
	v_add_u32_e32 v38, 0x8000, v67
	v_pk_mul_f32 v[78:79], v[78:79], v[92:93] op_sel_hi:[1,0]
	ds_write2_b32 v38, v80, v81 offset1:1
	v_add_u32_e32 v38, 0x8008, v67
	ds_write2_b32 v38, v78, v79 offset1:1
	v_pk_mul_f32 v[76:77], v[76:77], v[90:91] op_sel_hi:[1,0]
	v_add_u32_e32 v38, 0x8420, v67
	v_pk_mul_f32 v[72:73], v[72:73], v[90:91] op_sel_hi:[1,0]
	ds_write2_b32 v38, v76, v77 offset1:1
	v_add_u32_e32 v38, 0x8428, v67
	ds_write2_b32 v38, v72, v73 offset1:1
	v_pk_mul_f32 v[70:71], v[70:71], v[88:89] op_sel_hi:[1,0]
	v_add_u32_e32 v38, 0x8840, v67
	v_pk_mul_f32 v[68:69], v[68:69], v[88:89] op_sel_hi:[1,0]
	ds_write2_b32 v38, v70, v71 offset1:1
	v_add_u32_e32 v38, 0x8848, v67
	ds_write2_b32 v38, v68, v69 offset1:1
	v_pk_mul_f32 v[64:65], v[64:65], v[82:83] op_sel_hi:[1,0]
	v_add_u32_e32 v38, 0x8c60, v67
	v_pk_mul_f32 v[62:63], v[62:63], v[82:83] op_sel_hi:[1,0]
	ds_write2_b32 v38, v64, v65 offset1:1
	v_add_u32_e32 v38, 0x8c68, v67
	ds_write2_b32 v38, v62, v63 offset1:1
	v_pk_mul_f32 v[60:61], v[60:61], v[74:75] op_sel_hi:[1,0]
	v_add_u32_e32 v38, 0x9080, v67
	v_pk_mul_f32 v[58:59], v[58:59], v[74:75] op_sel_hi:[1,0]
	ds_write2_b32 v38, v60, v61 offset1:1
	v_add_u32_e32 v38, 0x9088, v67
	ds_write2_b32 v38, v58, v59 offset1:1
	v_pk_mul_f32 v[54:55], v[54:55], v[66:67] op_sel_hi:[1,0]
	v_add_u32_e32 v38, 0x94a0, v67
	v_pk_mul_f32 v[52:53], v[52:53], v[66:67] op_sel_hi:[1,0]
	ds_write2_b32 v38, v54, v55 offset1:1
	v_add_u32_e32 v38, 0x94a8, v67
	ds_write2_b32 v38, v52, v53 offset1:1
	v_pk_mul_f32 v[2:3], v[2:3], v[56:57] op_sel_hi:[1,0]
	v_add_u32_e32 v38, 0x98c0, v67
	v_pk_mul_f32 v[4:5], v[4:5], v[56:57] op_sel_hi:[1,0]
	ds_write2_b32 v38, v2, v3 offset1:1
	v_add_u32_e32 v2, 0x98c8, v67
	ds_write2_b32 v2, v4, v5 offset1:1
	s_waitcnt lgkmcnt(0)
	v_add_u32_e32 v38, 0x8000, v47
	ds_read2_b32 v[2:3], v38 offset1:33
	ds_read2_b32 v[4:5], v38 offset0:66 offset1:99
	ds_read2_b32 v[54:55], v38 offset0:132 offset1:165
	ds_read2_b32 v[58:59], v38 offset0:198 offset1:231
	v_mov_b32_e32 v51, v39
	v_lshl_add_u64 v[52:53], s[12:13], 0, v[50:51]
	s_cmp_lg_u32 s8, 0
	s_waitcnt lgkmcnt(3)
	v_cvt_pk_bf16_f32 v2, v2, v3
	s_waitcnt lgkmcnt(2)
	v_cvt_pk_bf16_f32 v3, v4, v5
	s_waitcnt lgkmcnt(1)
	v_cvt_pk_bf16_f32 v4, v54, v55
	v_mad_u64_u32 v[54:55], s[6:7], s36, v40, 0
	s_cselect_b64 s[12:13], -1, 0
	s_cmp_eq_u32 s8, 0
	s_waitcnt lgkmcnt(0)
	v_cvt_pk_bf16_f32 v5, v58, v59
	v_lshl_add_u64 v[54:55], v[54:55], 1, v[52:53]
	global_store_dwordx4 v[54:55], v[2:5], off sc1
	s_cbranch_scc1 .LBB0_100
	v_lshl_add_u64 v[54:55], s[8:9], 1, v[54:55]
	global_store_dwordx4 v[54:55], v[2:5], off sc1

.LBB0_215:
	v_pk_mul_f32 v[86:87], v[86:87], v[94:95] op_sel_hi:[1,0]
	v_add_u32_e32 v38, 0x8000, v57
	v_pk_mul_f32 v[84:85], v[84:85], v[94:95] op_sel_hi:[1,0]
	ds_write2_b32 v38, v86, v87 offset1:1
	v_add_u32_e32 v38, 0x8008, v57
	ds_write2_b32 v38, v84, v85 offset1:1
	v_pk_mul_f32 v[80:81], v[80:81], v[92:93] op_sel_hi:[1,0]
	v_add_u32_e32 v38, 0x8000, v67
	v_pk_mul_f32 v[78:79], v[78:79], v[92:93] op_sel_hi:[1,0]
	ds_write2_b32 v38, v80, v81 offset1:1
	v_add_u32_e32 v38, 0x8008, v67
	ds_write2_b32 v38, v78, v79 offset1:1
	v_pk_mul_f32 v[76:77], v[76:77], v[90:91] op_sel_hi:[1,0]
	v_add_u32_e32 v38, 0x8420, v67
	v_pk_mul_f32 v[72:73], v[72:73], v[90:91] op_sel_hi:[1,0]
	ds_write2_b32 v38, v76, v77 offset1:1
	v_add_u32_e32 v38, 0x8428, v67
	ds_write2_b32 v38, v72, v73 offset1:1
	v_pk_mul_f32 v[70:71], v[70:71], v[88:89] op_sel_hi:[1,0]
	v_add_u32_e32 v38, 0x8840, v67
	v_pk_mul_f32 v[68:69], v[68:69], v[88:89] op_sel_hi:[1,0]
	ds_write2_b32 v38, v70, v71 offset1:1
	v_add_u32_e32 v38, 0x8848, v67
	ds_write2_b32 v38, v68, v69 offset1:1
	v_pk_mul_f32 v[64:65], v[64:65], v[82:83] op_sel_hi:[1,0]
	v_add_u32_e32 v38, 0x8c60, v67
	v_pk_mul_f32 v[62:63], v[62:63], v[82:83] op_sel_hi:[1,0]
	ds_write2_b32 v38, v64, v65 offset1:1
	v_add_u32_e32 v38, 0x8c68, v67
	ds_write2_b32 v38, v62, v63 offset1:1
	v_pk_mul_f32 v[60:61], v[60:61], v[74:75] op_sel_hi:[1,0]
	v_add_u32_e32 v38, 0x9080, v67
	v_pk_mul_f32 v[58:59], v[58:59], v[74:75] op_sel_hi:[1,0]
	ds_write2_b32 v38, v60, v61 offset1:1
	v_add_u32_e32 v38, 0x9088, v67
	ds_write2_b32 v38, v58, v59 offset1:1
	v_pk_mul_f32 v[54:55], v[54:55], v[66:67] op_sel_hi:[1,0]
	v_add_u32_e32 v38, 0x94a0, v67
	v_pk_mul_f32 v[52:53], v[52:53], v[66:67] op_sel_hi:[1,0]
	ds_write2_b32 v38, v54, v55 offset1:1
	v_add_u32_e32 v38, 0x94a8, v67
	ds_write2_b32 v38, v52, v53 offset1:1
	v_pk_mul_f32 v[2:3], v[2:3], v[56:57] op_sel_hi:[1,0]
	v_add_u32_e32 v38, 0x98c0, v67
	v_pk_mul_f32 v[4:5], v[4:5], v[56:57] op_sel_hi:[1,0]
	ds_write2_b32 v38, v2, v3 offset1:1
	v_add_u32_e32 v2, 0x98c8, v67
	ds_write2_b32 v2, v4, v5 offset1:1
	s_waitcnt lgkmcnt(0)
	v_add_u32_e32 v38, 0x8000, v47
	ds_read2_b32 v[2:3], v38 offset1:33
	ds_read2_b32 v[4:5], v38 offset0:66 offset1:99
	ds_read2_b32 v[54:55], v38 offset0:132 offset1:165
	ds_read2_b32 v[58:59], v38 offset0:198 offset1:231
	v_mov_b32_e32 v51, v39
	v_lshl_add_u64 v[52:53], s[10:11], 0, v[50:51]
	s_cmp_lg_u32 s8, 0
	s_waitcnt lgkmcnt(3)
	v_cvt_pk_bf16_f32 v2, v2, v3
	s_waitcnt lgkmcnt(2)
	v_cvt_pk_bf16_f32 v3, v4, v5
	s_waitcnt lgkmcnt(1)
	v_cvt_pk_bf16_f32 v4, v54, v55
	v_mad_u64_u32 v[54:55], s[6:7], s27, v40, 0
	s_cselect_b64 s[10:11], -1, 0
	s_cmp_eq_u32 s8, 0
	s_waitcnt lgkmcnt(0)
	v_cvt_pk_bf16_f32 v5, v58, v59
	v_lshl_add_u64 v[54:55], v[54:55], 1, v[52:53]
	global_store_dwordx4 v[54:55], v[2:5], off sc1
	s_cbranch_scc1 .LBB0_217
	v_lshl_add_u64 v[54:55], s[8:9], 1, v[54:55]
	global_store_dwordx4 v[54:55], v[2:5], off sc1

.LBB0_584:
	v_pk_mul_f32 v[86:87], v[86:87], v[94:95] op_sel_hi:[1,0]
	v_add_u32_e32 v38, 0x8000, v57
	v_pk_mul_f32 v[84:85], v[84:85], v[94:95] op_sel_hi:[1,0]
	ds_write2_b32 v38, v86, v87 offset1:1
	v_add_u32_e32 v38, 0x8008, v57
	ds_write2_b32 v38, v84, v85 offset1:1
	v_pk_mul_f32 v[80:81], v[80:81], v[92:93] op_sel_hi:[1,0]
	v_add_u32_e32 v38, 0x8000, v67
	v_pk_mul_f32 v[78:79], v[78:79], v[92:93] op_sel_hi:[1,0]
	ds_write2_b32 v38, v80, v81 offset1:1
	v_add_u32_e32 v38, 0x8008, v67
	ds_write2_b32 v38, v78, v79 offset1:1
	v_pk_mul_f32 v[76:77], v[76:77], v[90:91] op_sel_hi:[1,0]
	v_add_u32_e32 v38, 0x8420, v67
	v_pk_mul_f32 v[74:75], v[74:75], v[90:91] op_sel_hi:[1,0]
	ds_write2_b32 v38, v76, v77 offset1:1
	v_add_u32_e32 v38, 0x8428, v67
	ds_write2_b32 v38, v74, v75 offset1:1
	v_pk_mul_f32 v[70:71], v[70:71], v[88:89] op_sel_hi:[1,0]
	v_add_u32_e32 v38, 0x8840, v67
	v_pk_mul_f32 v[68:69], v[68:69], v[88:89] op_sel_hi:[1,0]
	ds_write2_b32 v38, v70, v71 offset1:1
	v_add_u32_e32 v38, 0x8848, v67
	ds_write2_b32 v38, v68, v69 offset1:1
	v_pk_mul_f32 v[64:65], v[64:65], v[82:83] op_sel_hi:[1,0]
	v_add_u32_e32 v38, 0x8c60, v67
	v_pk_mul_f32 v[62:63], v[62:63], v[82:83] op_sel_hi:[1,0]
	ds_write2_b32 v38, v64, v65 offset1:1
	v_add_u32_e32 v38, 0x8c68, v67
	ds_write2_b32 v38, v62, v63 offset1:1
	v_pk_mul_f32 v[60:61], v[60:61], v[72:73] op_sel_hi:[1,0]
	v_add_u32_e32 v38, 0x9080, v67
	v_pk_mul_f32 v[58:59], v[58:59], v[72:73] op_sel_hi:[1,0]
	ds_write2_b32 v38, v60, v61 offset1:1
	v_add_u32_e32 v38, 0x9088, v67
	ds_write2_b32 v38, v58, v59 offset1:1
	v_pk_mul_f32 v[54:55], v[54:55], v[66:67] op_sel_hi:[1,0]
	v_add_u32_e32 v38, 0x94a0, v67
	v_pk_mul_f32 v[52:53], v[52:53], v[66:67] op_sel_hi:[1,0]
	ds_write2_b32 v38, v54, v55 offset1:1
	v_add_u32_e32 v38, 0x94a8, v67
	ds_write2_b32 v38, v52, v53 offset1:1
	v_pk_mul_f32 v[2:3], v[2:3], v[56:57] op_sel_hi:[1,0]
	v_add_u32_e32 v38, 0x98c0, v67
	v_pk_mul_f32 v[4:5], v[4:5], v[56:57] op_sel_hi:[1,0]
	ds_write2_b32 v38, v2, v3 offset1:1
	v_add_u32_e32 v2, 0x98c8, v67
	ds_write2_b32 v2, v4, v5 offset1:1
	s_waitcnt lgkmcnt(0)
	v_add_u32_e32 v38, 0x8000, v47
	ds_read2_b32 v[2:3], v38 offset1:33
	ds_read2_b32 v[4:5], v38 offset0:66 offset1:99
	ds_read2_b32 v[54:55], v38 offset0:132 offset1:165
	ds_read2_b32 v[58:59], v38 offset0:198 offset1:231
	v_mov_b32_e32 v51, v39
	v_lshl_add_u64 v[52:53], s[8:9], 0, v[50:51]
	s_cmp_lg_u32 s6, 0
	s_waitcnt lgkmcnt(3)
	v_cvt_pk_bf16_f32 v2, v2, v3
	s_waitcnt lgkmcnt(2)
	v_cvt_pk_bf16_f32 v3, v4, v5
	s_waitcnt lgkmcnt(1)
	v_cvt_pk_bf16_f32 v4, v54, v55
	v_mad_u64_u32 v[54:55], s[4:5], s35, v40, 0
	s_cselect_b64 s[8:9], -1, 0
	s_cmp_eq_u32 s6, 0
	s_waitcnt lgkmcnt(0)
	v_cvt_pk_bf16_f32 v5, v58, v59
	v_lshl_add_u64 v[54:55], v[54:55], 1, v[52:53]
	global_store_dwordx4 v[54:55], v[2:5], off sc1
	s_cbranch_scc1 .LBB0_586
	v_lshl_add_u64 v[54:55], s[6:7], 1, v[54:55]
	global_store_dwordx4 v[54:55], v[2:5], off sc1
